# baseline (speedup 1.0000x reference)
.LBB0_53:
	s_andn2_b64 vcc, exec, s[4:5]
	s_cbranch_vccnz .LBB0_59
	s_load_dwordx2 s[6:7], s[0:1], 0x8
	s_load_dwordx2 s[4:5], s[0:1], 0x40
	s_lshl_b32 s3, s2, 10
	s_add_i32 s3, s3, 0xfffc2c00
	v_or_b32_e32 v30, s3, v0
	v_lshlrev_b32_e32 v31, 5, v30
	v_lshlrev_b32_e32 v32, 4, v30
	v_add_u32_e32 v33, 0x800000, v31
	v_add_u32_e32 v34, 0x1000000, v31
	v_add_u32_e32 v35, 0x1800000, v31
	s_movk_i32 s8, 0x3500
	v_cmp_gt_u32_e32 vcc, s8, v30
	s_waitcnt lgkmcnt(0)
	global_load_dwordx4 v[2:5], v31, s[6:7] nt
	global_load_dwordx4 v[6:9], v31, s[6:7] offset:16 nt
	global_load_dwordx4 v[10:13], v33, s[6:7] nt
	global_load_dwordx4 v[14:17], v33, s[6:7] offset:16 nt
	global_load_dwordx4 v[18:21], v34, s[6:7] nt
	global_load_dwordx4 v[22:25], v34, s[6:7] offset:16 nt
	s_and_saveexec_b64 s[8:9], vcc
	s_cbranch_execz .Lk1c_a
	global_load_dwordx4 v[26:29], v35, s[6:7] nt
	global_load_dwordx4 v[36:39], v35, s[6:7] offset:16 nt
.Lk1c_a:
	s_mov_b64 exec, s[8:9]
	v_add_u32_e32 v33, 0x400000, v32
	v_add_u32_e32 v34, 0x800000, v32
	v_add_u32_e32 v35, 0xc00000, v32
	s_waitcnt vmcnt(0)
	v_cvt_pk_f16_f32 v2, v2, v3
	v_cvt_pk_f16_f32 v3, v4, v5
	v_cvt_pk_f16_f32 v4, v6, v7
	v_cvt_pk_f16_f32 v5, v8, v9
	global_store_dwordx4 v32, v[2:5], s[4:5] sc1
	v_cvt_pk_f16_f32 v10, v10, v11
	v_cvt_pk_f16_f32 v11, v12, v13
	v_cvt_pk_f16_f32 v12, v14, v15
	v_cvt_pk_f16_f32 v13, v16, v17
	global_store_dwordx4 v33, v[10:13], s[4:5] sc1
	v_cvt_pk_f16_f32 v18, v18, v19
	v_cvt_pk_f16_f32 v19, v20, v21
	v_cvt_pk_f16_f32 v20, v22, v23
	v_cvt_pk_f16_f32 v21, v24, v25
	global_store_dwordx4 v34, v[18:21], s[4:5] sc1
	s_and_saveexec_b64 s[8:9], vcc
	s_cbranch_execz .Lk1c_b
	v_cvt_pk_f16_f32 v26, v26, v27
	v_cvt_pk_f16_f32 v27, v28, v29
	v_cvt_pk_f16_f32 v28, v36, v37
	v_cvt_pk_f16_f32 v29, v38, v39
	global_store_dwordx4 v35, v[26:29], s[4:5] sc1
.Lk1c_b:
	s_mov_b64 exec, s[8:9]
